# nt hint on the Y8 stores of the down projection; router-logit MFMA section of the LayerNorm+router phase prefetches its LDS A-fragments two reads ahead through a 3-register ring instead of read-wait-u
# speedup vs baseline: 1.0017x; 1.0017x over previous
; #define LAS __attribute__((address_space(3)))
; DI int crow(int reg, int h) { return (reg & 3) + 8 * (reg >> 2) + 4 * h; }
; #define LN_SYNC() do { asm volatile("s_waitcnt lgkmcnt(0)" ::: "memory"); __builtin_amdgcn_s_barrier(); asm volatile("" ::: "memory"); } while (0)
; DI void phase_lnr(const Ctx& c, int layer) {
;     ...
;         {
;             f32x16 acc;
; #pragma unroll
;             for (int i = 0; i < 16; ++i) acc[i] = 0.f;
;             LAS const bf16_t* ah = AHI + r * LN_AP + kq * 256 + h * 8; LAS const bf16_t* al = ALO + r * LN_AP + kq * 256 + h * 8;
; #pragma unroll
;             for (int ks = 0; ks < 16; ++ks) {
;                 const bf16x8 a1 = *(const LAS bf16x8*)(ah + ks * 16), a2 = *(const LAS bf16x8*)(al + ks * 16);
;                 acc = __builtin_amdgcn_mfma_f32_32x32x16_bf16(a1, bhf[ks], acc, 0, 0, 0);
;                 acc = __builtin_amdgcn_mfma_f32_32x32x16_bf16(a1, blf[ks], acc, 0, 0, 0);
;                 acc = __builtin_amdgcn_mfma_f32_32x32x16_bf16(a2, bhf[ks], acc, 0, 0, 0);
;             }
;             LN_SYNC();
; #pragma unroll
;             for (int i = 0; i < 16; ++i) PART[(kq * 32 + crow(i, h)) * 65 + nt * 32 + r] = acc[i];
;         }
.LBB0_1031:
	s_waitcnt lgkmcnt(0)
	s_barrier
	ds_read_b128 v[178:181], v224
	ds_read_b128 v[242:245], v226
	ds_read_b128 v[248:251], v224 offset:32
	v_add_u32_e32 v176, 0x800, v240
	s_and_b64 s[0:1], s[0:1], exec
	s_cselect_b32 s47, 4, 2
	s_mov_b32 s48, 0
	s_waitcnt lgkmcnt(2)
	v_mfma_f32_32x32x16_bf16 v[0:15], v[178:181], v[16:19], 0
	v_mfma_f32_32x32x16_bf16 v[0:15], v[178:181], v[20:23], v[0:15]
	ds_read_b128 v[178:181], v226 offset:32
	s_waitcnt lgkmcnt(2)
	v_mfma_f32_32x32x16_bf16 v[0:15], v[242:245], v[16:19], v[0:15]
	ds_read_b128 v[242:245], v224 offset:64
	s_waitcnt lgkmcnt(2)
	v_mfma_f32_32x32x16_bf16 v[0:15], v[248:251], v[24:27], v[0:15]
	v_mfma_f32_32x32x16_bf16 v[0:15], v[248:251], v[128:131], v[0:15]
	ds_read_b128 v[248:251], v226 offset:64
	s_waitcnt lgkmcnt(2)
	v_mfma_f32_32x32x16_bf16 v[0:15], v[178:181], v[24:27], v[0:15]
	ds_read_b128 v[178:181], v224 offset:96
	s_waitcnt lgkmcnt(2)
	v_mfma_f32_32x32x16_bf16 v[0:15], v[242:245], v[28:31], v[0:15]
	v_mfma_f32_32x32x16_bf16 v[0:15], v[242:245], v[32:35], v[0:15]
	ds_read_b128 v[242:245], v226 offset:96
	s_waitcnt lgkmcnt(2)
	v_mfma_f32_32x32x16_bf16 v[0:15], v[248:251], v[28:31], v[0:15]
	ds_read_b128 v[248:251], v224 offset:128
	s_waitcnt lgkmcnt(2)
	v_mfma_f32_32x32x16_bf16 v[0:15], v[178:181], v[40:43], v[0:15]
	v_mfma_f32_32x32x16_bf16 v[0:15], v[178:181], v[36:39], v[0:15]
	ds_read_b128 v[178:181], v226 offset:128
	s_waitcnt lgkmcnt(2)
	v_mfma_f32_32x32x16_bf16 v[0:15], v[242:245], v[40:43], v[0:15]
	ds_read_b128 v[242:245], v224 offset:160
	s_waitcnt lgkmcnt(2)
	v_mfma_f32_32x32x16_bf16 v[0:15], v[248:251], v[44:47], v[0:15]
	v_mfma_f32_32x32x16_bf16 v[0:15], v[248:251], v[48:51], v[0:15]
	ds_read_b128 v[248:251], v226 offset:160
	s_waitcnt lgkmcnt(2)
	v_mfma_f32_32x32x16_bf16 v[0:15], v[178:181], v[44:47], v[0:15]
	ds_read_b128 v[178:181], v224 offset:192
	s_waitcnt lgkmcnt(2)
	v_mfma_f32_32x32x16_bf16 v[0:15], v[242:245], v[56:59], v[0:15]
	v_mfma_f32_32x32x16_bf16 v[0:15], v[242:245], v[52:55], v[0:15]
	ds_read_b128 v[242:245], v226 offset:192
	s_waitcnt lgkmcnt(2)
	v_mfma_f32_32x32x16_bf16 v[0:15], v[248:251], v[56:59], v[0:15]
	ds_read_b128 v[248:251], v224 offset:224
	s_waitcnt lgkmcnt(2)
	v_mfma_f32_32x32x16_bf16 v[0:15], v[178:181], v[60:63], v[0:15]
	v_mfma_f32_32x32x16_bf16 v[0:15], v[178:181], v[64:67], v[0:15]
	ds_read_b128 v[178:181], v226 offset:224
	s_waitcnt lgkmcnt(2)
	v_mfma_f32_32x32x16_bf16 v[0:15], v[242:245], v[60:63], v[0:15]
	ds_read_b128 v[242:245], v224 offset:256
	s_waitcnt lgkmcnt(2)
	v_mfma_f32_32x32x16_bf16 v[0:15], v[248:251], v[72:75], v[0:15]
	v_mfma_f32_32x32x16_bf16 v[0:15], v[248:251], v[68:71], v[0:15]
	ds_read_b128 v[248:251], v226 offset:256
	s_waitcnt lgkmcnt(2)
	v_mfma_f32_32x32x16_bf16 v[0:15], v[178:181], v[72:75], v[0:15]
	ds_read_b128 v[178:181], v224 offset:288
	s_waitcnt lgkmcnt(2)
	v_mfma_f32_32x32x16_bf16 v[0:15], v[242:245], v[76:79], v[0:15]
	v_mfma_f32_32x32x16_bf16 v[0:15], v[242:245], v[80:83], v[0:15]
	ds_read_b128 v[242:245], v226 offset:288
	s_waitcnt lgkmcnt(2)
	v_mfma_f32_32x32x16_bf16 v[0:15], v[248:251], v[76:79], v[0:15]
	ds_read_b128 v[248:251], v224 offset:320
	s_waitcnt lgkmcnt(2)
	v_mfma_f32_32x32x16_bf16 v[0:15], v[178:181], v[88:91], v[0:15]
	v_mfma_f32_32x32x16_bf16 v[0:15], v[178:181], v[84:87], v[0:15]
	ds_read_b128 v[178:181], v226 offset:320
	s_waitcnt lgkmcnt(2)
	v_mfma_f32_32x32x16_bf16 v[0:15], v[242:245], v[88:91], v[0:15]
	ds_read_b128 v[242:245], v224 offset:352
	s_waitcnt lgkmcnt(2)
	v_mfma_f32_32x32x16_bf16 v[0:15], v[248:251], v[92:95], v[0:15]
	v_mfma_f32_32x32x16_bf16 v[0:15], v[248:251], v[96:99], v[0:15]
	ds_read_b128 v[248:251], v226 offset:352
	s_waitcnt lgkmcnt(2)
	v_mfma_f32_32x32x16_bf16 v[0:15], v[178:181], v[92:95], v[0:15]
	ds_read_b128 v[178:181], v224 offset:384
	s_waitcnt lgkmcnt(2)
	v_mfma_f32_32x32x16_bf16 v[0:15], v[242:245], v[104:107], v[0:15]
	v_mfma_f32_32x32x16_bf16 v[0:15], v[242:245], v[100:103], v[0:15]
	ds_read_b128 v[242:245], v226 offset:384
	s_waitcnt lgkmcnt(2)
	v_mfma_f32_32x32x16_bf16 v[0:15], v[248:251], v[104:107], v[0:15]
	ds_read_b128 v[248:251], v224 offset:416
	s_waitcnt lgkmcnt(2)
	v_mfma_f32_32x32x16_bf16 v[0:15], v[178:181], v[108:111], v[0:15]
	v_mfma_f32_32x32x16_bf16 v[0:15], v[178:181], v[112:115], v[0:15]
	ds_read_b128 v[178:181], v226 offset:416
	s_waitcnt lgkmcnt(2)
	v_mfma_f32_32x32x16_bf16 v[0:15], v[242:245], v[108:111], v[0:15]
	ds_read_b128 v[242:245], v224 offset:448
	s_waitcnt lgkmcnt(2)
	v_mfma_f32_32x32x16_bf16 v[0:15], v[248:251], v[120:123], v[0:15]
	v_mfma_f32_32x32x16_bf16 v[0:15], v[248:251], v[116:119], v[0:15]
	ds_read_b128 v[248:251], v226 offset:448
	s_waitcnt lgkmcnt(2)
	v_mfma_f32_32x32x16_bf16 v[0:15], v[178:181], v[120:123], v[0:15]
	ds_read_b128 v[178:181], v224 offset:480
	s_waitcnt lgkmcnt(2)
	v_mfma_f32_32x32x16_bf16 v[0:15], v[242:245], v[124:127], v[0:15]
	v_mfma_f32_32x32x16_bf16 v[0:15], v[242:245], v[136:139], v[0:15]
	ds_read_b128 v[242:245], v226 offset:480
	s_waitcnt lgkmcnt(2)
	v_mfma_f32_32x32x16_bf16 v[0:15], v[248:251], v[124:127], v[0:15]
	s_waitcnt lgkmcnt(0)
	s_barrier
	v_mfma_f32_32x32x16_bf16 v[0:15], v[178:181], v[132:135], v[0:15]
	v_mfma_f32_32x32x16_bf16 v[0:15], v[178:181], v[140:143], v[0:15]
	v_add_u32_e32 v178, 0x1000, v240
	v_add_u32_e32 v179, 0x1800, v240
	v_mfma_f32_32x32x16_bf16 v[0:15], v[242:245], v[132:135], v[0:15]
	s_nop 11
	ds_write2_b32 v240, v0, v1 offset1:65
	ds_write2_b32 v240, v2, v3 offset0:130 offset1:195
	ds_write2_b32 v176, v4, v5 offset0:8 offset1:73
	ds_write2_b32 v176, v6, v7 offset0:138 offset1:203
	ds_write2_b32 v178, v8, v9 offset0:16 offset1:81
	ds_write2_b32 v178, v10, v11 offset0:146 offset1:211
	ds_write2_b32 v179, v12, v13 offset0:24 offset1:89
	ds_write2_b32 v179, v14, v15 offset0:154 offset1:219
	s_waitcnt lgkmcnt(0)
	s_barrier
	s_branch .LBB0_1033
